# MoE-up: ai=0 half of the SwiGLU epilogue interleaved with the last K-iteration's final MFMA phase (ai=1); post-loop epilogue keeps the ai=1 half
# baseline (speedup 1.0000x reference)
.LBB0_1389:
	s_add_u32 vcc_lo, s78, 0x100
	s_addc_u32 vcc_hi, s79, 0
	s_and_b64 s[38:39], s[40:41], exec
	s_cselect_b32 s76, 0, vcc_lo
	s_add_u32 s78, s91, s78
	s_addc_u32 s79, s46, s79
	s_waitcnt vmcnt(8)
	s_and_b64 s[38:39], s[40:41], exec
	s_waitcnt lgkmcnt(0)
	s_cselect_b32 s78, s94, s78
	s_cselect_b32 s79, s95, s79
	s_add_u32 s40, s78, 0x80
	s_addc_u32 s41, s79, 0
	s_barrier
	s_setprio 1
	s_waitcnt lgkmcnt(6)
	v_mfma_scale_f32_16x16x128_f8f6f4 v[190:193], v[18:25], v[58:65], v[190:193], v200, v200 op_sel_hi:[0,0,0]
	v_mfma_scale_f32_16x16x128_f8f6f4 v[182:185], v[26:33], v[58:65], v[182:185], v200, v200 op_sel_hi:[0,0,0]
	s_waitcnt lgkmcnt(4)
	v_mfma_scale_f32_16x16x128_f8f6f4 v[174:177], v[18:25], v[50:57], v[174:177], v200, v200 op_sel_hi:[0,0,0]
	v_mfma_scale_f32_16x16x128_f8f6f4 v[166:169], v[26:33], v[50:57], v[166:169], v200, v200 op_sel_hi:[0,0,0]
	s_waitcnt lgkmcnt(2)
	v_mfma_scale_f32_16x16x128_f8f6f4 v[158:161], v[18:25], v[42:49], v[158:161], v200, v200 op_sel_hi:[0,0,0]
	v_mfma_scale_f32_16x16x128_f8f6f4 v[150:153], v[26:33], v[42:49], v[150:153], v200, v200 op_sel_hi:[0,0,0]
	s_waitcnt lgkmcnt(0)
	v_mfma_scale_f32_16x16x128_f8f6f4 v[142:145], v[18:25], v[34:41], v[142:145], v200, v200 op_sel_hi:[0,0,0]
	v_mfma_scale_f32_16x16x128_f8f6f4 v[134:137], v[26:33], v[34:41], v[134:137], v200, v200 op_sel_hi:[0,0,0]
	s_setprio 0
	s_setprio 1
	v_mfma_scale_f32_16x16x128_f8f6f4 v[186:189], v[2:9], v[58:65], v[186:189], v200, v200 op_sel_hi:[0,0,0]
	v_mfma_scale_f32_16x16x128_f8f6f4 v[178:181], v[10:17], v[58:65], v[178:181], v200, v200 op_sel_hi:[0,0,0]
	v_mfma_scale_f32_16x16x128_f8f6f4 v[170:173], v[2:9], v[50:57], v[170:173], v200, v200 op_sel_hi:[0,0,0]
	v_mfma_scale_f32_16x16x128_f8f6f4 v[162:165], v[10:17], v[50:57], v[162:165], v200, v200 op_sel_hi:[0,0,0]
	v_mfma_scale_f32_16x16x128_f8f6f4 v[154:157], v[2:9], v[42:49], v[154:157], v200, v200 op_sel_hi:[0,0,0]
	v_mfma_scale_f32_16x16x128_f8f6f4 v[146:149], v[10:17], v[42:49], v[146:149], v200, v200 op_sel_hi:[0,0,0]
	v_mfma_scale_f32_16x16x128_f8f6f4 v[138:141], v[2:9], v[34:41], v[138:141], v200, v200 op_sel_hi:[0,0,0]
	v_mfma_scale_f32_16x16x128_f8f6f4 v[130:133], v[10:17], v[34:41], v[130:133], v200, v200 op_sel_hi:[0,0,0]
	s_setprio 0
	s_barrier
	ds_read_b128 v[34:37], v216 offset:16384
	ds_read_b128 v[38:41], v216 offset:16400
	ds_read_b128 v[46:49], v216 offset:18448
	ds_read_b128 v[42:45], v216 offset:18432
	ds_read_b128 v[54:57], v216 offset:20496
	ds_read_b128 v[50:53], v216 offset:20480
	ds_read_b128 v[62:65], v216 offset:22544
	ds_read_b128 v[58:61], v216 offset:22528
	s_mov_b32 m0, s48
	s_nop 0
	global_load_lds_dwordx4 v208, s[78:79]
	s_add_u32 s38, s78, 0x10000
	s_addc_u32 s39, s79, 0
	s_mov_b32 m0, s49
	s_nop 0
	global_load_lds_dwordx4 v208, s[38:39]
	s_add_u32 s38, s78, 0x20000
	s_addc_u32 s39, s79, 0
	s_mov_b32 m0, s26
	s_nop 0
	global_load_lds_dwordx4 v208, s[38:39]
	s_add_u32 s38, s38, 0x10000
	s_addc_u32 s39, s39, 0
	s_mov_b32 m0, s0
	s_nop 0
	global_load_lds_dwordx4 v208, s[38:39]
	s_add_u32 s38, s62, s76
	s_addc_u32 s39, s63, 0
	s_mov_b32 m0, s51
	s_nop 0
	global_load_lds_dwordx4 v211, s[38:39]
	s_nop 0
	s_mov_b32 m0, s1
	s_nop 0
	global_load_lds_dwordx4 v213, s[38:39]
	s_waitcnt vmcnt(8)
	s_waitcnt lgkmcnt(0)
	s_barrier
	s_setprio 1
	s_waitcnt lgkmcnt(6)
	v_mfma_scale_f32_16x16x128_f8f6f4 v[126:129], v[18:25], v[34:41], v[126:129], v200, v200 op_sel_hi:[0,0,0]
	v_mfma_scale_f32_16x16x128_f8f6f4 v[118:121], v[26:33], v[34:41], v[118:121], v200, v200 op_sel_hi:[0,0,0]
	s_waitcnt lgkmcnt(4)
	v_mfma_scale_f32_16x16x128_f8f6f4 v[110:113], v[18:25], v[42:49], v[110:113], v200, v200 op_sel_hi:[0,0,0]
	v_mfma_scale_f32_16x16x128_f8f6f4 v[102:105], v[26:33], v[42:49], v[102:105], v200, v200 op_sel_hi:[0,0,0]
	s_waitcnt lgkmcnt(2)
	v_mfma_scale_f32_16x16x128_f8f6f4 v[94:97], v[18:25], v[50:57], v[94:97], v200, v200 op_sel_hi:[0,0,0]
	v_mfma_scale_f32_16x16x128_f8f6f4 v[86:89], v[26:33], v[50:57], v[86:89], v200, v200 op_sel_hi:[0,0,0]
	s_waitcnt lgkmcnt(0)
	v_mfma_scale_f32_16x16x128_f8f6f4 v[78:81], v[18:25], v[58:65], v[78:81], v200, v200 op_sel_hi:[0,0,0]
	v_mfma_scale_f32_16x16x128_f8f6f4 v[70:73], v[26:33], v[58:65], v[70:73], v200, v200 op_sel_hi:[0,0,0]
	s_setprio 0
	s_setprio 1
	v_mfma_scale_f32_16x16x128_f8f6f4 v[122:125], v[2:9], v[34:41], v[122:125], v200, v200 op_sel_hi:[0,0,0]
	v_mfma_scale_f32_16x16x128_f8f6f4 v[114:117], v[10:17], v[34:41], v[114:117], v200, v200 op_sel_hi:[0,0,0]
	v_mfma_scale_f32_16x16x128_f8f6f4 v[106:109], v[2:9], v[42:49], v[106:109], v200, v200 op_sel_hi:[0,0,0]
	v_mfma_scale_f32_16x16x128_f8f6f4 v[98:101], v[10:17], v[42:49], v[98:101], v200, v200 op_sel_hi:[0,0,0]
	v_mfma_scale_f32_16x16x128_f8f6f4 v[90:93], v[2:9], v[50:57], v[90:93], v200, v200 op_sel_hi:[0,0,0]
	v_mfma_scale_f32_16x16x128_f8f6f4 v[82:85], v[10:17], v[50:57], v[82:85], v200, v200 op_sel_hi:[0,0,0]
	v_mfma_scale_f32_16x16x128_f8f6f4 v[74:77], v[2:9], v[58:65], v[74:77], v200, v200 op_sel_hi:[0,0,0]
	v_mfma_scale_f32_16x16x128_f8f6f4 v[66:69], v[10:17], v[58:65], v[66:69], v200, v200 op_sel_hi:[0,0,0]
	s_setprio 0
	s_barrier
	v_add_u32_e32 v10, 0x18000, v215
	v_add_u32_e32 v26, 0x1c000, v215
	ds_read_b128 v[2:5], v10
	ds_read_b128 v[6:9], v10 offset:16
	ds_read_b128 v[14:17], v10 offset:2064
	ds_read_b128 v[10:13], v10 offset:2048
	ds_read_b128 v[18:21], v26
	ds_read_b128 v[22:25], v26 offset:16
	ds_read_b128 v[30:33], v26 offset:2064
	ds_read_b128 v[26:29], v26 offset:2048
	ds_read_b128 v[34:37], v216 offset:32768
	ds_read_b128 v[38:41], v216 offset:32784
	ds_read_b128 v[46:49], v216 offset:34832
	ds_read_b128 v[42:45], v216 offset:34816
	ds_read_b128 v[54:57], v216 offset:36880
	ds_read_b128 v[50:53], v216 offset:36864
	ds_read_b128 v[62:65], v216 offset:38928
	ds_read_b128 v[58:61], v216 offset:38912
	s_mov_b32 m0, s16
	s_nop 0
	global_load_lds_dwordx4 v212, s[38:39]
	s_nop 0
	s_mov_b32 m0, s17
	s_nop 0
	global_load_lds_dwordx4 v214, s[38:39]
	s_waitcnt vmcnt(8)
	s_waitcnt lgkmcnt(0)
	s_barrier
	s_setprio 1
	s_waitcnt lgkmcnt(6)
	v_mfma_scale_f32_16x16x128_f8f6f4 v[190:193], v[2:9], v[34:41], v[190:193], v200, v200 op_sel_hi:[0,0,0]
	v_mfma_scale_f32_16x16x128_f8f6f4 v[182:185], v[10:17], v[34:41], v[182:185], v200, v200 op_sel_hi:[0,0,0]
	s_waitcnt lgkmcnt(4)
	v_mfma_scale_f32_16x16x128_f8f6f4 v[174:177], v[2:9], v[42:49], v[174:177], v200, v200 op_sel_hi:[0,0,0]
	v_mfma_scale_f32_16x16x128_f8f6f4 v[166:169], v[10:17], v[42:49], v[166:169], v200, v200 op_sel_hi:[0,0,0]
	s_waitcnt lgkmcnt(2)
	v_mfma_scale_f32_16x16x128_f8f6f4 v[158:161], v[2:9], v[50:57], v[158:161], v200, v200 op_sel_hi:[0,0,0]
	v_mfma_scale_f32_16x16x128_f8f6f4 v[150:153], v[10:17], v[50:57], v[150:153], v200, v200 op_sel_hi:[0,0,0]
	s_waitcnt lgkmcnt(0)
	v_mfma_scale_f32_16x16x128_f8f6f4 v[142:145], v[2:9], v[58:65], v[142:145], v200, v200 op_sel_hi:[0,0,0]
	v_mfma_scale_f32_16x16x128_f8f6f4 v[134:137], v[10:17], v[58:65], v[134:137], v200, v200 op_sel_hi:[0,0,0]
	s_setprio 0
	s_setprio 1
	v_mfma_scale_f32_16x16x128_f8f6f4 v[186:189], v[18:25], v[34:41], v[186:189], v200, v200 op_sel_hi:[0,0,0]
	v_mfma_scale_f32_16x16x128_f8f6f4 v[178:181], v[26:33], v[34:41], v[178:181], v200, v200 op_sel_hi:[0,0,0]
	v_mfma_scale_f32_16x16x128_f8f6f4 v[170:173], v[18:25], v[42:49], v[170:173], v200, v200 op_sel_hi:[0,0,0]
	v_mfma_scale_f32_16x16x128_f8f6f4 v[162:165], v[26:33], v[42:49], v[162:165], v200, v200 op_sel_hi:[0,0,0]
	v_mfma_scale_f32_16x16x128_f8f6f4 v[154:157], v[18:25], v[50:57], v[154:157], v200, v200 op_sel_hi:[0,0,0]
	v_mfma_scale_f32_16x16x128_f8f6f4 v[146:149], v[26:33], v[50:57], v[146:149], v200, v200 op_sel_hi:[0,0,0]
	v_mfma_scale_f32_16x16x128_f8f6f4 v[138:141], v[18:25], v[58:65], v[138:141], v200, v200 op_sel_hi:[0,0,0]
	v_mfma_scale_f32_16x16x128_f8f6f4 v[130:133], v[26:33], v[58:65], v[130:133], v200, v200 op_sel_hi:[0,0,0]
	s_setprio 0
	s_barrier
	ds_read_b128 v[34:37], v216 offset:49152
	ds_read_b128 v[38:41], v216 offset:49168
	ds_read_b128 v[46:49], v216 offset:51216
	ds_read_b128 v[42:45], v216 offset:51200
	ds_read_b128 v[54:57], v216 offset:53264
	ds_read_b128 v[50:53], v216 offset:53248
	ds_read_b128 v[62:65], v216 offset:55312
	ds_read_b128 v[58:61], v216 offset:55296
	s_mov_b32 m0, s14
	s_nop 0
	global_load_lds_dwordx4 v208, s[40:41]
	s_add_u32 s40, s40, 0x10000
	s_addc_u32 s41, s41, 0
	s_mov_b32 m0, s15
	s_nop 0
	global_load_lds_dwordx4 v208, s[40:41]
	s_add_u32 s40, s78, 0x20080
	s_addc_u32 s41, s79, 0
	s_mov_b32 m0, s64
	s_nop 0
	global_load_lds_dwordx4 v208, s[40:41]
	s_add_u32 s40, s40, 0x10000
	s_addc_u32 s41, s41, 0
	s_mov_b32 m0, s65
	s_nop 0
	global_load_lds_dwordx4 v208, s[40:41]
	s_add_u32 s38, s38, 0x80
	s_addc_u32 s39, s39, 0
	s_mov_b32 m0, s34
	s_nop 0
	global_load_lds_dwordx4 v211, s[38:39]
	s_nop 0
	s_mov_b32 m0, s19
	s_nop 0
	global_load_lds_dwordx4 v213, s[38:39]
	s_waitcnt vmcnt(8)
	s_waitcnt lgkmcnt(0)
	s_barrier
	s_cmp_eq_u32 s88, 4
	s_cbranch_scc1 .Lepi_moe_last
	s_setprio 1
	s_waitcnt lgkmcnt(6)
	v_mfma_scale_f32_16x16x128_f8f6f4 v[126:129], v[2:9], v[34:41], v[126:129], v200, v200 op_sel_hi:[0,0,0]
	v_mfma_scale_f32_16x16x128_f8f6f4 v[118:121], v[10:17], v[34:41], v[118:121], v200, v200 op_sel_hi:[0,0,0]
	s_waitcnt lgkmcnt(4)
	v_mfma_scale_f32_16x16x128_f8f6f4 v[110:113], v[2:9], v[42:49], v[110:113], v200, v200 op_sel_hi:[0,0,0]
	v_mfma_scale_f32_16x16x128_f8f6f4 v[102:105], v[10:17], v[42:49], v[102:105], v200, v200 op_sel_hi:[0,0,0]
	s_waitcnt lgkmcnt(2)
	v_mfma_scale_f32_16x16x128_f8f6f4 v[94:97], v[2:9], v[50:57], v[94:97], v200, v200 op_sel_hi:[0,0,0]
	v_mfma_scale_f32_16x16x128_f8f6f4 v[86:89], v[10:17], v[50:57], v[86:89], v200, v200 op_sel_hi:[0,0,0]
	s_waitcnt lgkmcnt(0)
	v_mfma_scale_f32_16x16x128_f8f6f4 v[78:81], v[2:9], v[58:65], v[78:81], v200, v200 op_sel_hi:[0,0,0]
	v_mfma_scale_f32_16x16x128_f8f6f4 v[70:73], v[10:17], v[58:65], v[70:73], v200, v200 op_sel_hi:[0,0,0]
	s_setprio 0
	s_setprio 1
	v_mfma_scale_f32_16x16x128_f8f6f4 v[122:125], v[18:25], v[34:41], v[122:125], v200, v200 op_sel_hi:[0,0,0]
	v_mfma_scale_f32_16x16x128_f8f6f4 v[114:117], v[26:33], v[34:41], v[114:117], v200, v200 op_sel_hi:[0,0,0]
	v_mfma_scale_f32_16x16x128_f8f6f4 v[106:109], v[18:25], v[42:49], v[106:109], v200, v200 op_sel_hi:[0,0,0]
	v_mfma_scale_f32_16x16x128_f8f6f4 v[98:101], v[26:33], v[42:49], v[98:101], v200, v200 op_sel_hi:[0,0,0]
	v_mfma_scale_f32_16x16x128_f8f6f4 v[90:93], v[18:25], v[50:57], v[90:93], v200, v200 op_sel_hi:[0,0,0]
	v_mfma_scale_f32_16x16x128_f8f6f4 v[82:85], v[26:33], v[50:57], v[82:85], v200, v200 op_sel_hi:[0,0,0]
	v_mfma_scale_f32_16x16x128_f8f6f4 v[74:77], v[18:25], v[58:65], v[74:77], v200, v200 op_sel_hi:[0,0,0]
	v_mfma_scale_f32_16x16x128_f8f6f4 v[66:69], v[26:33], v[58:65], v[66:69], v200, v200 op_sel_hi:[0,0,0]
	s_setprio 0
	s_barrier
	s_add_i32 s88, s88, 2
	s_cmp_gt_u32 s88, 5
	s_cbranch_scc1 .LBB0_1391
	s_mov_b64 s[78:79], vcc
	s_branch .LBB0_1387
.Lepi_moe_last:
	s_setprio 1
	v_mfma_scale_f32_16x16x128_f8f6f4 v[126:129], v[2:9], v[34:41], v[126:129], v200, v200 op_sel_hi:[0,0,0]
	s_lshl_b32 s38, s42, 8
	v_mov_b32_e32 v252, v0
	s_add_i32 s38, s38, s31
	s_mov_b32 s98, 0xbfb8aa3b
	v_and_or_b32 v253, v252, 15, s38
	s_lshl_b32 s38, s45, 7
	s_ashr_i32 s39, s38, 31
	v_lshrrev_b32_e32 v252, 1, v252
	s_add_u32 s38, s5, s38
	v_and_or_b32 v250, v252, 24, s25
	v_mov_b32_e32 v251, 0
	s_addc_u32 s39, s4, s39
	v_lshl_add_u64 v[250:251], s[38:39], 0, v[250:251]
	v_mfma_scale_f32_16x16x128_f8f6f4 v[118:121], v[10:17], v[34:41], v[118:121], v200, v200 op_sel_hi:[0,0,0]
	s_mov_b32 s101, 0
	v_mad_i64_i32 v[250:251], s[38:39], v253, s2, v[250:251]
	v_pk_mul_f32 v[218:219], v[190:191], s[98:99] op_sel_hi:[1,0]
	v_pk_mul_f32 v[220:221], v[192:193], s[98:99] op_sel_hi:[1,0]
	v_exp_f32_e32 v218, v218
	v_pk_mul_f32 v[222:223], v[182:183], s[98:99] op_sel_hi:[1,0]
	v_pk_mul_f32 v[224:225], v[184:185], s[98:99] op_sel_hi:[1,0]
	v_exp_f32_e32 v219, v219
	v_pk_mul_f32 v[228:229], v[174:175], s[98:99] op_sel_hi:[1,0]
	v_pk_mul_f32 v[230:231], v[176:177], s[98:99] op_sel_hi:[1,0]
	v_exp_f32_e32 v220, v220
	v_pk_mul_f32 v[232:233], v[166:167], s[98:99] op_sel_hi:[1,0]
	v_pk_fma_f32 v[218:219], v[218:219], s[66:67], s[66:67] op_sel_hi:[1,0,0]
	v_mfma_scale_f32_16x16x128_f8f6f4 v[110:113], v[2:9], v[42:49], v[110:113], v200, v200 op_sel_hi:[0,0,0]
	v_exp_f32_e32 v221, v221
	v_pk_mul_f32 v[234:235], v[168:169], s[98:99] op_sel_hi:[1,0]
	s_mul_i32 s100, s2, 0x10
	v_exp_f32_e32 v222, v222
	v_lshl_add_u64 v[248:249], s[100:101], 0, v[250:251]
	v_pk_fma_f32 v[220:221], v[220:221], s[66:67], s[66:67] op_sel_hi:[1,0,0]
	v_exp_f32_e32 v223, v223
	v_pk_mul_f32 v[238:239], v[158:159], s[98:99] op_sel_hi:[1,0]
	v_pk_mul_f32 v[240:241], v[160:161], s[98:99] op_sel_hi:[1,0]
	v_exp_f32_e32 v224, v224
	v_pk_mul_f32 v[242:243], v[150:151], s[98:99] op_sel_hi:[1,0]
	v_pk_fma_f32 v[222:223], v[222:223], s[66:67], s[66:67] op_sel_hi:[1,0,0]
	v_mfma_scale_f32_16x16x128_f8f6f4 v[102:105], v[10:17], v[42:49], v[102:105], v200, v200 op_sel_hi:[0,0,0]
	v_exp_f32_e32 v225, v225
	v_pk_mul_f32 v[244:245], v[152:153], s[98:99] op_sel_hi:[1,0]
	s_mul_i32 s100, s2, 0x20
	v_rcp_f32_e32 v218, v218
	v_rcp_f32_e32 v219, v219
	v_pk_fma_f32 v[224:225], v[224:225], s[66:67], s[66:67] op_sel_hi:[1,0,0]
	v_rcp_f32_e32 v220, v220
	v_rcp_f32_e32 v221, v221
	v_rcp_f32_e32 v222, v222
	v_pk_mul_f32 v[218:219], v[190:191], v[218:219]
	v_rcp_f32_e32 v223, v223
	v_pk_mul_f32 v[218:219], v[218:219], v[186:187]
	v_pk_mul_f32 v[220:221], v[192:193], v[220:221]
	v_mfma_scale_f32_16x16x128_f8f6f4 v[94:97], v[2:9], v[50:57], v[94:97], v200, v200 op_sel_hi:[0,0,0]
	v_rcp_f32_e32 v224, v224
	v_pk_mul_f32 v[220:221], v[220:221], v[188:189]
	v_pk_mul_f32 v[222:223], v[182:183], v[222:223]
	v_rcp_f32_e32 v225, v225
	v_pk_mul_f32 v[222:223], v[222:223], v[178:179]
	v_med3_f32 v218, v218, s29, v1
	v_exp_f32_e32 v228, v228
	v_med3_f32 v219, v219, s29, v1
	v_pk_mul_f32 v[224:225], v[184:185], v[224:225]
	v_exp_f32_e32 v229, v229
	v_pk_mul_f32 v[224:225], v[224:225], v[180:181]
	v_med3_f32 v220, v220, s29, v1
	v_exp_f32_e32 v230, v230
	v_mfma_scale_f32_16x16x128_f8f6f4 v[86:89], v[10:17], v[50:57], v[86:89], v200, v200 op_sel_hi:[0,0,0]
	v_med3_f32 v221, v221, s29, v1
	v_med3_f32 v222, v222, s29, v1
	v_exp_f32_e32 v231, v231
	v_med3_f32 v223, v223, s29, v1
	v_med3_f32 v224, v224, s29, v1
	v_exp_f32_e32 v232, v232
	v_med3_f32 v225, v225, s29, v1
	v_cvt_pk_fp8_f32 v226, v218, v219
	v_exp_f32_e32 v233, v233
	v_cvt_pk_fp8_f32 v227, v222, v223
	v_cvt_pk_fp8_f32 v226, v220, v221 op_sel:[0,0,1]
	v_exp_f32_e32 v234, v234
	v_mfma_scale_f32_16x16x128_f8f6f4 v[78:81], v[2:9], v[58:65], v[78:81], v200, v200 op_sel_hi:[0,0,0]
	v_cvt_pk_fp8_f32 v227, v224, v225 op_sel:[0,0,1]
	v_pk_fma_f32 v[228:229], v[228:229], s[66:67], s[66:67] op_sel_hi:[1,0,0]
	v_exp_f32_e32 v235, v235
	global_store_dwordx2 v[250:251], v[226:227], off
	v_pk_fma_f32 v[230:231], v[230:231], s[66:67], s[66:67] op_sel_hi:[1,0,0]
	v_rcp_f32_e32 v228, v228
	v_pk_fma_f32 v[232:233], v[232:233], s[66:67], s[66:67] op_sel_hi:[1,0,0]
	v_pk_fma_f32 v[234:235], v[234:235], s[66:67], s[66:67] op_sel_hi:[1,0,0]
	v_rcp_f32_e32 v229, v229
	v_pk_mul_f32 v[218:219], v[142:143], s[98:99] op_sel_hi:[1,0]
	v_pk_mul_f32 v[220:221], v[144:145], s[98:99] op_sel_hi:[1,0]
	v_rcp_f32_e32 v230, v230
	v_pk_mul_f32 v[222:223], v[134:135], s[98:99] op_sel_hi:[1,0]
	v_mfma_scale_f32_16x16x128_f8f6f4 v[70:73], v[10:17], v[58:65], v[70:73], v200, v200 op_sel_hi:[0,0,0]
	v_pk_mul_f32 v[228:229], v[174:175], v[228:229]
	v_rcp_f32_e32 v231, v231
	v_pk_mul_f32 v[228:229], v[228:229], v[170:171]
	v_pk_mul_f32 v[224:225], v[136:137], s[98:99] op_sel_hi:[1,0]
	v_rcp_f32_e32 v232, v232
	v_med3_f32 v228, v228, s29, v1
	v_pk_mul_f32 v[230:231], v[176:177], v[230:231]
	v_rcp_f32_e32 v233, v233
	v_pk_mul_f32 v[230:231], v[230:231], v[172:173]
	v_med3_f32 v229, v229, s29, v1
	v_rcp_f32_e32 v234, v234
	v_med3_f32 v230, v230, s29, v1
	v_mfma_scale_f32_16x16x128_f8f6f4 v[122:125], v[18:25], v[34:41], v[122:125], v200, v200 op_sel_hi:[0,0,0]
	v_pk_mul_f32 v[232:233], v[166:167], v[232:233]
	v_rcp_f32_e32 v235, v235
	v_pk_mul_f32 v[232:233], v[232:233], v[162:163]
	v_med3_f32 v231, v231, s29, v1
	v_exp_f32_e32 v238, v238
	v_med3_f32 v232, v232, s29, v1
	v_pk_mul_f32 v[234:235], v[168:169], v[234:235]
	v_exp_f32_e32 v239, v239
	v_pk_mul_f32 v[234:235], v[234:235], v[164:165]
	v_med3_f32 v233, v233, s29, v1
	v_exp_f32_e32 v240, v240
	v_med3_f32 v234, v234, s29, v1
	v_med3_f32 v235, v235, s29, v1
	v_mfma_scale_f32_16x16x128_f8f6f4 v[114:117], v[26:33], v[34:41], v[114:117], v200, v200 op_sel_hi:[0,0,0]
	v_exp_f32_e32 v241, v241
	v_cvt_pk_fp8_f32 v236, v228, v229
	v_cvt_pk_fp8_f32 v237, v232, v233
	v_exp_f32_e32 v242, v242
	v_cvt_pk_fp8_f32 v236, v230, v231 op_sel:[0,0,1]
	v_cvt_pk_fp8_f32 v237, v234, v235 op_sel:[0,0,1]
	v_exp_f32_e32 v243, v243
	global_store_dwordx2 v[248:249], v[236:237], off
	v_pk_fma_f32 v[238:239], v[238:239], s[66:67], s[66:67] op_sel_hi:[1,0,0]
	v_exp_f32_e32 v244, v244
	v_pk_fma_f32 v[240:241], v[240:241], s[66:67], s[66:67] op_sel_hi:[1,0,0]
	v_pk_fma_f32 v[242:243], v[242:243], s[66:67], s[66:67] op_sel_hi:[1,0,0]
	v_exp_f32_e32 v245, v245
	v_mfma_scale_f32_16x16x128_f8f6f4 v[106:109], v[18:25], v[42:49], v[106:109], v200, v200 op_sel_hi:[0,0,0]
	v_lshl_add_u64 v[248:249], s[100:101], 0, v[250:251]
	s_mul_i32 s100, s2, 0x30
	v_rcp_f32_e32 v238, v238
	v_rcp_f32_e32 v239, v239
	v_pk_fma_f32 v[244:245], v[244:245], s[66:67], s[66:67] op_sel_hi:[1,0,0]
	v_rcp_f32_e32 v240, v240
	v_rcp_f32_e32 v241, v241
	v_rcp_f32_e32 v242, v242
	v_pk_mul_f32 v[238:239], v[158:159], v[238:239]
	v_rcp_f32_e32 v243, v243
	v_pk_mul_f32 v[238:239], v[238:239], v[154:155]
	v_pk_mul_f32 v[240:241], v[160:161], v[240:241]
	v_mfma_scale_f32_16x16x128_f8f6f4 v[98:101], v[26:33], v[42:49], v[98:101], v200, v200 op_sel_hi:[0,0,0]
	v_rcp_f32_e32 v244, v244
	v_pk_mul_f32 v[240:241], v[240:241], v[156:157]
	v_pk_mul_f32 v[242:243], v[150:151], v[242:243]
	v_rcp_f32_e32 v245, v245
	v_pk_mul_f32 v[242:243], v[242:243], v[146:147]
	v_med3_f32 v238, v238, s29, v1
	v_exp_f32_e32 v218, v218
	v_med3_f32 v239, v239, s29, v1
	v_pk_mul_f32 v[244:245], v[152:153], v[244:245]
	v_exp_f32_e32 v219, v219
	v_pk_mul_f32 v[244:245], v[244:245], v[148:149]
	v_med3_f32 v240, v240, s29, v1
	v_exp_f32_e32 v220, v220
	v_mfma_scale_f32_16x16x128_f8f6f4 v[90:93], v[18:25], v[50:57], v[90:93], v200, v200 op_sel_hi:[0,0,0]
	v_med3_f32 v241, v241, s29, v1
	v_med3_f32 v242, v242, s29, v1
	v_exp_f32_e32 v221, v221
	v_med3_f32 v243, v243, s29, v1
	v_med3_f32 v244, v244, s29, v1
	v_exp_f32_e32 v222, v222
	v_med3_f32 v245, v245, s29, v1
	v_cvt_pk_fp8_f32 v246, v238, v239
	v_exp_f32_e32 v223, v223
	v_cvt_pk_fp8_f32 v247, v242, v243
	v_cvt_pk_fp8_f32 v246, v240, v241 op_sel:[0,0,1]
	v_exp_f32_e32 v224, v224
	v_cvt_pk_fp8_f32 v247, v244, v245 op_sel:[0,0,1]
	v_mfma_scale_f32_16x16x128_f8f6f4 v[82:85], v[26:33], v[50:57], v[82:85], v200, v200 op_sel_hi:[0,0,0]
	v_pk_fma_f32 v[218:219], v[218:219], s[66:67], s[66:67] op_sel_hi:[1,0,0]
	v_exp_f32_e32 v225, v225
	global_store_dwordx2 v[248:249], v[246:247], off
	v_pk_fma_f32 v[220:221], v[220:221], s[66:67], s[66:67] op_sel_hi:[1,0,0]
	v_rcp_f32_e32 v218, v218
	v_pk_fma_f32 v[222:223], v[222:223], s[66:67], s[66:67] op_sel_hi:[1,0,0]
	v_pk_fma_f32 v[224:225], v[224:225], s[66:67], s[66:67] op_sel_hi:[1,0,0]
	v_rcp_f32_e32 v219, v219
	v_lshl_add_u64 v[248:249], s[100:101], 0, v[250:251]
	v_rcp_f32_e32 v220, v220
	v_rcp_f32_e32 v221, v221
	v_rcp_f32_e32 v222, v222
	v_mfma_scale_f32_16x16x128_f8f6f4 v[74:77], v[18:25], v[58:65], v[74:77], v200, v200 op_sel_hi:[0,0,0]
	v_pk_mul_f32 v[218:219], v[142:143], v[218:219]
	v_rcp_f32_e32 v223, v223
	v_pk_mul_f32 v[218:219], v[218:219], v[138:139]
	v_pk_mul_f32 v[220:221], v[144:145], v[220:221]
	v_rcp_f32_e32 v224, v224
	v_pk_mul_f32 v[220:221], v[220:221], v[140:141]
	v_pk_mul_f32 v[222:223], v[134:135], v[222:223]
	v_rcp_f32_e32 v225, v225
	v_pk_mul_f32 v[222:223], v[222:223], v[130:131]
	v_med3_f32 v218, v218, s29, v1
	v_med3_f32 v219, v219, s29, v1
	v_med3_f32 v220, v220, s29, v1
	v_pk_mul_f32 v[224:225], v[136:137], v[224:225]
	v_mfma_scale_f32_16x16x128_f8f6f4 v[66:69], v[26:33], v[58:65], v[66:69], v200, v200 op_sel_hi:[0,0,0]
	v_med3_f32 v221, v221, s29, v1
	v_pk_mul_f32 v[224:225], v[224:225], v[132:133]
	v_med3_f32 v222, v222, s29, v1
	v_med3_f32 v223, v223, s29, v1
	v_med3_f32 v224, v224, s29, v1
	v_med3_f32 v225, v225, s29, v1
	v_cvt_pk_fp8_f32 v226, v218, v219
	v_cvt_pk_fp8_f32 v227, v222, v223
	v_cvt_pk_fp8_f32 v226, v220, v221 op_sel:[0,0,1]
	v_cvt_pk_fp8_f32 v227, v224, v225 op_sel:[0,0,1]
	s_nop 0
	global_store_dwordx2 v[248:249], v[226:227], off
	s_setprio 0
	s_barrier

.LBB0_1393:
	s_lshl_b32 s38, s42, 8
	v_mov_b32_e32 v2, v0
	s_add_i32 s38, s38, s31
	s_mov_b32 s98, 0xbfb8aa3b
	v_and_or_b32 v4, v2, 15, s38
	s_lshl_b32 s38, s45, 7
	s_ashr_i32 s39, s38, 31
	v_lshrrev_b32_e32 v2, 1, v2
	s_add_u32 s38, s5, s38
	v_and_or_b32 v194, v2, 24, s25
	s_addc_u32 s39, s4, s39
	v_lshl_add_u64 v[2:3], s[38:39], 0, v[194:195]
	s_andn2_b64 vcc, exec, s[92:93]
	s_mov_b32 s101, 0
	v_mad_i64_i32 v[2:3], s[38:39], v4, s2, v[2:3]
	v_pk_mul_f32 v[6:7], v[126:127], s[98:99] op_sel_hi:[1,0]
	v_pk_mul_f32 v[8:9], v[128:129], s[98:99] op_sel_hi:[1,0]
	v_exp_f32_e32 v6, v6
	v_pk_mul_f32 v[10:11], v[118:119], s[98:99] op_sel_hi:[1,0]
	v_pk_mul_f32 v[12:13], v[120:121], s[98:99] op_sel_hi:[1,0]
	v_exp_f32_e32 v7, v7
	s_mul_i32 s100, s2, 0x80
	v_pk_mul_f32 v[18:19], v[110:111], s[98:99] op_sel_hi:[1,0]
	v_exp_f32_e32 v8, v8
	v_lshl_add_u64 v[16:17], s[100:101], 0, v[2:3]
	v_pk_fma_f32 v[6:7], v[6:7], s[66:67], s[66:67] op_sel_hi:[1,0,0]
	v_exp_f32_e32 v9, v9
	v_pk_mul_f32 v[20:21], v[112:113], s[98:99] op_sel_hi:[1,0]
	v_pk_mul_f32 v[22:23], v[102:103], s[98:99] op_sel_hi:[1,0]
	v_exp_f32_e32 v10, v10
	v_pk_mul_f32 v[24:25], v[104:105], s[98:99] op_sel_hi:[1,0]
	v_pk_fma_f32 v[8:9], v[8:9], s[66:67], s[66:67] op_sel_hi:[1,0,0]
	v_exp_f32_e32 v11, v11
	s_mul_i32 s100, s2, 0x90
	v_pk_mul_f32 v[30:31], v[94:95], s[98:99] op_sel_hi:[1,0]
	v_exp_f32_e32 v12, v12
	v_lshl_add_u64 v[28:29], s[100:101], 0, v[2:3]
	v_pk_fma_f32 v[10:11], v[10:11], s[66:67], s[66:67] op_sel_hi:[1,0,0]
	v_exp_f32_e32 v13, v13
	v_pk_mul_f32 v[32:33], v[96:97], s[98:99] op_sel_hi:[1,0]
	v_pk_mul_f32 v[34:35], v[86:87], s[98:99] op_sel_hi:[1,0]
	v_rcp_f32_e32 v6, v6
	v_pk_mul_f32 v[36:37], v[88:89], s[98:99] op_sel_hi:[1,0]
	v_pk_fma_f32 v[12:13], v[12:13], s[66:67], s[66:67] op_sel_hi:[1,0,0]
	v_rcp_f32_e32 v7, v7
	s_mul_i32 s100, s2, 0xa0
	v_pk_mul_f32 v[42:43], v[78:79], s[98:99] op_sel_hi:[1,0]
	v_rcp_f32_e32 v8, v8
	v_lshl_add_u64 v[40:41], s[100:101], 0, v[2:3]
	v_pk_mul_f32 v[6:7], v[126:127], v[6:7]
	v_rcp_f32_e32 v9, v9
	v_pk_mul_f32 v[6:7], v[6:7], v[122:123]
	v_pk_mul_f32 v[44:45], v[80:81], s[98:99] op_sel_hi:[1,0]
	v_rcp_f32_e32 v10, v10
	v_med3_f32 v6, v6, s29, v1
	v_pk_mul_f32 v[8:9], v[128:129], v[8:9]
	v_rcp_f32_e32 v11, v11
	v_pk_mul_f32 v[8:9], v[8:9], v[124:125]
	v_med3_f32 v7, v7, s29, v1
	v_rcp_f32_e32 v12, v12
	v_med3_f32 v8, v8, s29, v1
	v_pk_mul_f32 v[10:11], v[118:119], v[10:11]
	v_rcp_f32_e32 v13, v13
	v_pk_mul_f32 v[10:11], v[10:11], v[114:115]
	v_med3_f32 v9, v9, s29, v1
	v_exp_f32_e32 v18, v18
	v_med3_f32 v10, v10, s29, v1
	v_pk_mul_f32 v[12:13], v[120:121], v[12:13]
	v_exp_f32_e32 v19, v19
	v_pk_mul_f32 v[12:13], v[12:13], v[116:117]
	v_med3_f32 v11, v11, s29, v1
	v_exp_f32_e32 v20, v20
	v_med3_f32 v12, v12, s29, v1
	v_med3_f32 v13, v13, s29, v1
	v_exp_f32_e32 v21, v21
	v_cvt_pk_fp8_f32 v14, v6, v7
	v_cvt_pk_fp8_f32 v15, v10, v11
	v_exp_f32_e32 v22, v22
	v_cvt_pk_fp8_f32 v14, v8, v9 op_sel:[0,0,1]
	v_cvt_pk_fp8_f32 v15, v12, v13 op_sel:[0,0,1]
	v_exp_f32_e32 v23, v23
	global_store_dwordx2 v[16:17], v[14:15], off
	v_pk_fma_f32 v[18:19], v[18:19], s[66:67], s[66:67] op_sel_hi:[1,0,0]
	v_exp_f32_e32 v24, v24
	v_pk_fma_f32 v[20:21], v[20:21], s[66:67], s[66:67] op_sel_hi:[1,0,0]
	v_pk_fma_f32 v[22:23], v[22:23], s[66:67], s[66:67] op_sel_hi:[1,0,0]
	v_exp_f32_e32 v25, v25
	v_pk_mul_f32 v[46:47], v[70:71], s[98:99] op_sel_hi:[1,0]
	v_pk_mul_f32 v[48:49], v[72:73], s[98:99] op_sel_hi:[1,0]
	v_rcp_f32_e32 v18, v18
	s_mul_i32 s100, s2, 0xb0
	v_pk_fma_f32 v[24:25], v[24:25], s[66:67], s[66:67] op_sel_hi:[1,0,0]
	v_rcp_f32_e32 v19, v19
	v_lshl_add_u64 v[52:53], s[100:101], 0, v[2:3]
	v_rcp_f32_e32 v20, v20
	v_rcp_f32_e32 v21, v21
	v_rcp_f32_e32 v22, v22
	v_pk_mul_f32 v[18:19], v[110:111], v[18:19]
	v_rcp_f32_e32 v23, v23
	v_pk_mul_f32 v[18:19], v[18:19], v[106:107]
	v_pk_mul_f32 v[20:21], v[112:113], v[20:21]
	v_rcp_f32_e32 v24, v24
	v_pk_mul_f32 v[20:21], v[20:21], v[108:109]
	v_pk_mul_f32 v[22:23], v[102:103], v[22:23]
	v_rcp_f32_e32 v25, v25
	v_pk_mul_f32 v[22:23], v[22:23], v[98:99]
	v_med3_f32 v18, v18, s29, v1
	v_exp_f32_e32 v30, v30
	v_med3_f32 v19, v19, s29, v1
	v_pk_mul_f32 v[24:25], v[104:105], v[24:25]
	v_exp_f32_e32 v31, v31
	v_pk_mul_f32 v[24:25], v[24:25], v[100:101]
	v_med3_f32 v20, v20, s29, v1
	v_exp_f32_e32 v32, v32
	v_med3_f32 v21, v21, s29, v1
	v_med3_f32 v22, v22, s29, v1
	v_exp_f32_e32 v33, v33
	v_med3_f32 v23, v23, s29, v1
	v_med3_f32 v24, v24, s29, v1
	v_exp_f32_e32 v34, v34
	v_med3_f32 v25, v25, s29, v1
	v_cvt_pk_fp8_f32 v26, v18, v19
	v_exp_f32_e32 v35, v35
	v_cvt_pk_fp8_f32 v27, v22, v23
	v_cvt_pk_fp8_f32 v26, v20, v21 op_sel:[0,0,1]
	v_exp_f32_e32 v36, v36
	v_cvt_pk_fp8_f32 v27, v24, v25 op_sel:[0,0,1]
	v_pk_fma_f32 v[30:31], v[30:31], s[66:67], s[66:67] op_sel_hi:[1,0,0]
	v_exp_f32_e32 v37, v37
	global_store_dwordx2 v[28:29], v[26:27], off
	v_pk_fma_f32 v[32:33], v[32:33], s[66:67], s[66:67] op_sel_hi:[1,0,0]
	v_rcp_f32_e32 v30, v30
	v_pk_fma_f32 v[34:35], v[34:35], s[66:67], s[66:67] op_sel_hi:[1,0,0]
	v_pk_fma_f32 v[36:37], v[36:37], s[66:67], s[66:67] op_sel_hi:[1,0,0]
	v_rcp_f32_e32 v31, v31
	v_rcp_f32_e32 v32, v32
	v_rcp_f32_e32 v33, v33
	v_rcp_f32_e32 v34, v34
	v_rcp_f32_e32 v35, v35
	v_pk_mul_f32 v[30:31], v[94:95], v[30:31]
	v_rcp_f32_e32 v36, v36
	v_pk_mul_f32 v[32:33], v[96:97], v[32:33]
	v_pk_mul_f32 v[30:31], v[30:31], v[90:91]
	v_rcp_f32_e32 v37, v37
	v_pk_mul_f32 v[34:35], v[86:87], v[34:35]
	v_pk_mul_f32 v[32:33], v[32:33], v[92:93]
	v_exp_f32_e32 v42, v42
	v_pk_mul_f32 v[34:35], v[34:35], v[82:83]
	v_pk_mul_f32 v[36:37], v[88:89], v[36:37]
	v_exp_f32_e32 v43, v43
	v_pk_mul_f32 v[36:37], v[36:37], v[84:85]
	v_med3_f32 v30, v30, s29, v1
	v_exp_f32_e32 v44, v44
	v_med3_f32 v31, v31, s29, v1
	v_med3_f32 v32, v32, s29, v1
	v_exp_f32_e32 v45, v45
	v_med3_f32 v33, v33, s29, v1
	v_med3_f32 v34, v34, s29, v1
	v_exp_f32_e32 v46, v46
	v_med3_f32 v35, v35, s29, v1
	v_med3_f32 v36, v36, s29, v1
	v_exp_f32_e32 v47, v47
	v_med3_f32 v37, v37, s29, v1
	v_cvt_pk_fp8_f32 v38, v30, v31
	v_exp_f32_e32 v48, v48
	v_cvt_pk_fp8_f32 v39, v34, v35
	v_cvt_pk_fp8_f32 v38, v32, v33 op_sel:[0,0,1]
	v_exp_f32_e32 v49, v49
	v_cvt_pk_fp8_f32 v39, v36, v37 op_sel:[0,0,1]
	v_pk_fma_f32 v[42:43], v[42:43], s[66:67], s[66:67] op_sel_hi:[1,0,0]
	global_store_dwordx2 v[40:41], v[38:39], off
	v_rcp_f32_e32 v42, v42
	v_pk_fma_f32 v[44:45], v[44:45], s[66:67], s[66:67] op_sel_hi:[1,0,0]
	v_pk_fma_f32 v[46:47], v[46:47], s[66:67], s[66:67] op_sel_hi:[1,0,0]
	v_rcp_f32_e32 v43, v43
	v_pk_fma_f32 v[48:49], v[48:49], s[66:67], s[66:67] op_sel_hi:[1,0,0]
	v_rcp_f32_e32 v44, v44
	v_rcp_f32_e32 v45, v45
	v_rcp_f32_e32 v46, v46
	v_pk_mul_f32 v[42:43], v[78:79], v[42:43]
	v_rcp_f32_e32 v47, v47
	v_pk_mul_f32 v[42:43], v[42:43], v[74:75]
	v_pk_mul_f32 v[44:45], v[80:81], v[44:45]
	v_rcp_f32_e32 v48, v48
	v_pk_mul_f32 v[44:45], v[44:45], v[76:77]
	v_pk_mul_f32 v[46:47], v[70:71], v[46:47]
	v_rcp_f32_e32 v49, v49
	v_pk_mul_f32 v[46:47], v[46:47], v[66:67]
	v_med3_f32 v42, v42, s29, v1
	v_med3_f32 v43, v43, s29, v1
	v_med3_f32 v44, v44, s29, v1
	v_pk_mul_f32 v[48:49], v[72:73], v[48:49]
	v_med3_f32 v45, v45, s29, v1
	v_pk_mul_f32 v[48:49], v[48:49], v[68:69]
	v_med3_f32 v46, v46, s29, v1
	v_med3_f32 v47, v47, s29, v1
	v_med3_f32 v48, v48, s29, v1
	v_med3_f32 v49, v49, s29, v1
	v_cvt_pk_fp8_f32 v50, v42, v43
	v_cvt_pk_fp8_f32 v51, v46, v47
	v_cvt_pk_fp8_f32 v50, v44, v45 op_sel:[0,0,1]
	v_cvt_pk_fp8_f32 v51, v48, v49 op_sel:[0,0,1]
	s_nop 0
	global_store_dwordx2 v[52:53], v[50:51], off
	s_mov_b64 s[38:39], -1
	s_cbranch_vccnz .LBB0_1362
	s_andn2_b64 vcc, exec, s[80:81]
	s_cbranch_vccnz .LBB0_1361
	s_barrier
	s_branch .LBB0_1361
